# speedup vs baseline: 1.0181x; 1.0181x over previous
_Z12score_kernelPKfP15HIP_vector_typeIjLj2EES0_S0_:
	s_load_dwordx4 s[4:7], s[0:1], 0x0
	s_load_dwordx4 s[32:35], s[0:1], 0x10
	s_and_b32 s15, s2, 7
	s_lshl_b32 s15, s15, 2
	s_lshr_b32 s17, s2, 6
	s_add_u32 s15, s15, s17
	s_bfe_u32 s16, s2, 0x30003
	s_mul_i32 s17, s16, 0x271
	v_add_u32_e32 v2, s17, v0
	v_lshlrev_b32_e32 v1, 2, v2
	s_movk_i32 s17, 0x271
	v_cmp_gt_u32_e32 vcc, s17, v0
	v_readfirstlane_b32 s21, v0
	s_and_b64 exec, exec, vcc
	s_mov_b64 s[18:19], exec
	s_lshr_b32 s21, s21, 6
	s_movk_i32 s13, 0x4e20
	s_mov_b32 s14, 0x3fb8aa3b
	s_mov_b32 s12, 0
	s_mov_b32 s10, 0x13d620
	s_mov_b32 s11, 0x20000
	s_mul_i32 s17, s15, 0x13d620
	s_mul_hi_u32 s20, s15, 0x13d620
	s_cmp_lg_u32 s21, 0
	s_cbranch_scc1 .Lk1_nowarm0
	s_getpc_b64 s[30:31]
	v_lshlrev_b32_e32 v3, 6, v0
	global_load_dword v92, v3, s[30:31]
	s_add_u32 s30, s30, 0x1000
	s_addc_u32 s31, s31, 0
	global_load_dword v93, v3, s[30:31]
	s_add_u32 s30, s30, 0x1000
	s_addc_u32 s31, s31, 0
	global_load_dword v94, v3, s[30:31]
	s_and_b32 s30, s0, 0xfffff000
	s_mov_b32 s31, s1
	global_load_dword v95, v3, s[30:31]
.Lk1_nowarm0:
	s_waitcnt lgkmcnt(0)
	s_add_u32 s8, s4, s17
	s_addc_u32 s9, s5, s20
	s_and_b32 s9, s9, 0xffff
	s_cmp_eq_u32 s21, 9
	s_cselect_b32 s17, 1, 0
	s_cmp_eq_u32 s16, 0
	s_cselect_b32 s17, s17, 0
	s_cmp_lg_u32 s17, 0
	s_cbranch_scc0 .Lk1_nowarm9
	s_mul_i32 s22, s15, 0x3a9800
	v_writelane_b32 v3, s22, 0
	s_add_u32 s23, s22, 0x10000
	v_writelane_b32 v3, s23, 1
	s_add_u32 s22, s22, 0x138800
	v_writelane_b32 v3, s22, 2
	s_add_u32 s23, s22, 0x10000
	v_writelane_b32 v3, s23, 3
	s_add_u32 s22, s22, 0x138800
	v_writelane_b32 v3, s22, 4
	s_add_u32 s23, s22, 0x10000
	v_writelane_b32 v3, s23, 5
	s_mov_b64 exec, 63
	global_load_dword v92, v3, s[32:33]
	s_mul_i32 s22, s15, 0x12c00
	s_add_u32 s22, s22, 0x1c200
	v_writelane_b32 v3, s22, 0
	s_add_u32 s22, s22, 0x10000
	v_writelane_b32 v3, s22, 1
	s_mul_i32 s22, s15, 0xe10
	v_writelane_b32 v3, s22, 2
	s_mul_i32 s22, s15, 0x4b0
	s_add_u32 s22, s22, 0x274200
	v_writelane_b32 v3, s22, 3
	s_mov_b64 exec, 15
	global_load_dword v93, v3, s[34:35]
	s_lshl_b32 s22, s15, 2
	s_add_u32 s22, s22, 0x138800
	v_mov_b32_e32 v3, s22
	v_mov_b32_e32 v81, 0
	s_mov_b64 exec, 1
	global_store_dword v3, v81, s[6:7]
	s_mov_b64 exec, s[18:19]
.Lk1_nowarm9:
	s_mov_b32 s40, 0
	s_add_u32 s41, s40, s13
	s_add_u32 s42, s41, s13
	s_add_u32 s43, s42, s13
	s_add_u32 s44, s43, s13
	s_add_u32 s45, s44, s13
	s_add_u32 s46, s45, s13
	s_add_u32 s47, s46, s13
	s_add_u32 s48, s47, s13
	s_add_u32 s49, s48, s13
	s_add_u32 s50, s49, s13
	s_add_u32 s51, s50, s13
	s_add_u32 s52, s51, s13
	s_add_u32 s53, s52, s13
	s_add_u32 s54, s53, s13
	s_add_u32 s55, s54, s13
	buffer_load_dword v8, v1, s[8:11], s40 offen nt
	buffer_load_dword v9, v1, s[8:11], s41 offen nt
	buffer_load_dword v10, v1, s[8:11], s42 offen nt
	buffer_load_dword v11, v1, s[8:11], s43 offen nt
	buffer_load_dword v12, v1, s[8:11], s44 offen nt
	buffer_load_dword v13, v1, s[8:11], s45 offen nt
	buffer_load_dword v14, v1, s[8:11], s46 offen nt
	buffer_load_dword v15, v1, s[8:11], s47 offen nt
	buffer_load_dword v16, v1, s[8:11], s48 offen nt
	buffer_load_dword v17, v1, s[8:11], s49 offen nt
	buffer_load_dword v18, v1, s[8:11], s50 offen nt
	buffer_load_dword v19, v1, s[8:11], s51 offen nt
	buffer_load_dword v20, v1, s[8:11], s52 offen nt
	buffer_load_dword v21, v1, s[8:11], s53 offen nt
	buffer_load_dword v22, v1, s[8:11], s54 offen nt
	buffer_load_dword v23, v1, s[8:11], s55 offen nt
	s_add_u32 s8, s8, 0x4e200
	s_addc_u32 s9, s9, 0
	buffer_load_dword v24, v1, s[8:11], s40 offen nt
	buffer_load_dword v25, v1, s[8:11], s41 offen nt
	buffer_load_dword v26, v1, s[8:11], s42 offen nt
	buffer_load_dword v27, v1, s[8:11], s43 offen nt
	buffer_load_dword v28, v1, s[8:11], s44 offen nt
	buffer_load_dword v29, v1, s[8:11], s45 offen nt
	buffer_load_dword v30, v1, s[8:11], s46 offen nt
	buffer_load_dword v31, v1, s[8:11], s47 offen nt
	buffer_load_dword v32, v1, s[8:11], s48 offen nt
	buffer_load_dword v33, v1, s[8:11], s49 offen nt
	buffer_load_dword v34, v1, s[8:11], s50 offen nt
	buffer_load_dword v35, v1, s[8:11], s51 offen nt
	buffer_load_dword v36, v1, s[8:11], s52 offen nt
	buffer_load_dword v37, v1, s[8:11], s53 offen nt
	buffer_load_dword v38, v1, s[8:11], s54 offen nt
	buffer_load_dword v39, v1, s[8:11], s55 offen nt
	s_add_u32 s8, s8, 0x4e200
	s_addc_u32 s9, s9, 0
	buffer_load_dword v40, v1, s[8:11], s40 offen nt
	buffer_load_dword v41, v1, s[8:11], s41 offen nt
	buffer_load_dword v42, v1, s[8:11], s42 offen nt
	buffer_load_dword v43, v1, s[8:11], s43 offen nt
	buffer_load_dword v44, v1, s[8:11], s44 offen nt
	buffer_load_dword v45, v1, s[8:11], s45 offen nt
	buffer_load_dword v46, v1, s[8:11], s46 offen nt
	buffer_load_dword v47, v1, s[8:11], s47 offen nt
	buffer_load_dword v48, v1, s[8:11], s48 offen nt
	buffer_load_dword v49, v1, s[8:11], s49 offen nt
	buffer_load_dword v50, v1, s[8:11], s50 offen nt
	buffer_load_dword v51, v1, s[8:11], s51 offen nt
	buffer_load_dword v52, v1, s[8:11], s52 offen nt
	buffer_load_dword v53, v1, s[8:11], s53 offen nt
	buffer_load_dword v54, v1, s[8:11], s54 offen nt
	buffer_load_dword v55, v1, s[8:11], s55 offen nt
	v_mul_u32_u24_e32 v3, 0x147b, v2
	v_lshrrev_b32_e32 v3, 19, v3
	v_mul_u32_u24_e32 v98, 0x64, v3
	v_sub_u32_e32 v98, v2, v98
	v_add_u32_e32 v3, -1, v3
	v_add_u32_e32 v98, -1, v98
	s_movk_i32 s17, 0x62
	v_cmp_gt_u32_e64 s[36:37], 48, v3
	v_cmp_gt_u32_e64 s[38:39], s17, v98
	s_mul_i32 s17, s15, 0x1388
	v_add_lshl_u32 v98, v2, s17, 3
	s_and_b64 s[36:37], s[36:37], s[38:39]
	s_waitcnt vmcnt(32)
	v_max3_f32 v76, v8, v9, v10
	v_max3_f32 v76, v76, v11, v12
	v_max3_f32 v76, v76, v13, v14
	v_max3_f32 v76, v76, v15, v16
	v_max3_f32 v76, v76, v17, v18
	v_max3_f32 v76, v76, v19, v20
	v_max3_f32 v76, v76, v21, v22
	v_max_f32_e32 v76, v76, v23
	v_sub_f32_e32 v8, v8, v76
	v_sub_f32_e32 v9, v9, v76
	v_sub_f32_e32 v10, v10, v76
	v_sub_f32_e32 v11, v11, v76
	v_sub_f32_e32 v12, v12, v76
	v_sub_f32_e32 v13, v13, v76
	v_sub_f32_e32 v14, v14, v76
	v_sub_f32_e32 v15, v15, v76
	v_sub_f32_e32 v16, v16, v76
	v_sub_f32_e32 v17, v17, v76
	v_sub_f32_e32 v18, v18, v76
	v_sub_f32_e32 v19, v19, v76
	v_sub_f32_e32 v20, v20, v76
	v_sub_f32_e32 v21, v21, v76
	v_sub_f32_e32 v22, v22, v76
	v_sub_f32_e32 v23, v23, v76
	v_or_b32_e32 v81, 0, v8
	v_or_b32_e32 v82, 1, v9
	v_min_u32_e32 v80, v81, v82
	v_or_b32_e32 v81, 2, v10
	v_or_b32_e32 v82, 3, v11
	v_min3_u32 v80, v80, v81, v82
	v_or_b32_e32 v81, 4, v12
	v_or_b32_e32 v82, 5, v13
	v_min3_u32 v80, v80, v81, v82
	v_or_b32_e32 v81, 6, v14
	v_or_b32_e32 v82, 7, v15
	v_min3_u32 v80, v80, v81, v82
	v_or_b32_e32 v81, 8, v16
	v_or_b32_e32 v82, 9, v17
	v_min3_u32 v80, v80, v81, v82
	v_or_b32_e32 v81, 10, v18
	v_or_b32_e32 v82, 11, v19
	v_min3_u32 v80, v80, v81, v82
	v_or_b32_e32 v81, 12, v20
	v_or_b32_e32 v82, 13, v21
	v_min3_u32 v80, v80, v81, v82
	v_or_b32_e32 v81, 14, v22
	v_or_b32_e32 v82, 15, v23
	v_min3_u32 v80, v80, v81, v82
	v_mul_f32_e32 v8, s14, v8
	v_mul_f32_e32 v9, s14, v9
	v_mul_f32_e32 v10, s14, v10
	v_mul_f32_e32 v11, s14, v11
	v_mul_f32_e32 v12, s14, v12
	v_mul_f32_e32 v13, s14, v13
	v_mul_f32_e32 v14, s14, v14
	v_mul_f32_e32 v15, s14, v15
	v_mul_f32_e32 v16, s14, v16
	v_mul_f32_e32 v17, s14, v17
	v_mul_f32_e32 v18, s14, v18
	v_mul_f32_e32 v19, s14, v19
	v_mul_f32_e32 v20, s14, v20
	v_mul_f32_e32 v21, s14, v21
	v_mul_f32_e32 v22, s14, v22
	v_mul_f32_e32 v23, s14, v23
	v_exp_f32_e32 v8, v8
	v_exp_f32_e32 v9, v9
	v_exp_f32_e32 v10, v10
	v_exp_f32_e32 v11, v11
	v_exp_f32_e32 v12, v12
	v_exp_f32_e32 v13, v13
	v_exp_f32_e32 v14, v14
	v_exp_f32_e32 v15, v15
	v_exp_f32_e32 v16, v16
	v_exp_f32_e32 v17, v17
	v_exp_f32_e32 v18, v18
	v_exp_f32_e32 v19, v19
	v_exp_f32_e32 v20, v20
	v_exp_f32_e32 v21, v21
	v_exp_f32_e32 v22, v22
	v_exp_f32_e32 v23, v23
	v_add_f32_e32 v78, v8, v10
	v_add_f32_e32 v79, v9, v11
	v_add_f32_e32 v78, v78, v12
	v_add_f32_e32 v79, v79, v13
	v_add_f32_e32 v78, v78, v14
	v_add_f32_e32 v79, v79, v15
	v_add_f32_e32 v78, v78, v16
	v_add_f32_e32 v79, v79, v17
	v_add_f32_e32 v78, v78, v18
	v_add_f32_e32 v79, v79, v19
	v_add_f32_e32 v78, v78, v20
	v_add_f32_e32 v79, v79, v21
	v_add_f32_e32 v78, v78, v22
	v_add_f32_e32 v79, v79, v23
	v_add_f32_e32 v78, v78, v79
	v_cvt_f64_f32_e32 v[86:87], v78
	v_mov_b32_e32 v75, v80
	v_mov_b32_e32 v73, v76
	s_add_u32 s8, s8, 0x4e200
	s_addc_u32 s9, s9, 0
	buffer_load_dword v56, v1, s[8:11], s40 offen nt
	buffer_load_dword v57, v1, s[8:11], s41 offen nt
	buffer_load_dword v58, v1, s[8:11], s42 offen nt
	buffer_load_dword v59, v1, s[8:11], s43 offen nt
	buffer_load_dword v60, v1, s[8:11], s44 offen nt
	buffer_load_dword v61, v1, s[8:11], s45 offen nt
	buffer_load_dword v62, v1, s[8:11], s46 offen nt
	buffer_load_dword v63, v1, s[8:11], s47 offen nt
	buffer_load_dword v64, v1, s[8:11], s48 offen nt
	buffer_load_dword v65, v1, s[8:11], s49 offen nt
	buffer_load_dword v66, v1, s[8:11], s50 offen nt
	buffer_load_dword v67, v1, s[8:11], s51 offen nt
	buffer_load_dword v68, v1, s[8:11], s52 offen nt
	buffer_load_dword v69, v1, s[8:11], s53 offen nt
	buffer_load_dword v70, v1, s[8:11], s54 offen nt
	buffer_load_dword v71, v1, s[8:11], s55 offen nt
	s_add_u32 s8, s8, 0x4e200
	s_addc_u32 s9, s9, 0
	buffer_load_dword v72, v1, s[8:11], s40 offen nt
	s_waitcnt vmcnt(33)
	v_max3_f32 v76, v24, v25, v26
	v_max3_f32 v76, v76, v27, v28
	v_max3_f32 v76, v76, v29, v30
	v_max3_f32 v76, v76, v31, v32
	v_max3_f32 v76, v76, v33, v34
	v_max3_f32 v76, v76, v35, v36
	v_max3_f32 v76, v76, v37, v38
	v_max_f32_e32 v76, v76, v39
	v_max_f32_e32 v77, v73, v76
	v_cmp_gt_f32_e64 s[20:21], v76, v73
	v_sub_f32_e32 v83, v73, v77
	v_mul_f32_e32 v83, s14, v83
	v_exp_f32_e32 v83, v83
	v_sub_f32_e32 v24, v24, v77
	v_sub_f32_e32 v25, v25, v77
	v_sub_f32_e32 v26, v26, v77
	v_sub_f32_e32 v27, v27, v77
	v_sub_f32_e32 v28, v28, v77
	v_sub_f32_e32 v29, v29, v77
	v_sub_f32_e32 v30, v30, v77
	v_sub_f32_e32 v31, v31, v77
	v_sub_f32_e32 v32, v32, v77
	v_sub_f32_e32 v33, v33, v77
	v_sub_f32_e32 v34, v34, v77
	v_sub_f32_e32 v35, v35, v77
	v_sub_f32_e32 v36, v36, v77
	v_sub_f32_e32 v37, v37, v77
	v_sub_f32_e32 v38, v38, v77
	v_sub_f32_e32 v39, v39, v77
	v_cvt_f64_f32_e32 v[84:85], v83
	v_or_b32_e32 v81, 16, v24
	v_or_b32_e32 v82, 17, v25
	v_min_u32_e32 v80, v81, v82
	v_or_b32_e32 v81, 18, v26
	v_or_b32_e32 v82, 19, v27
	v_min3_u32 v80, v80, v81, v82
	v_or_b32_e32 v81, 20, v28
	v_or_b32_e32 v82, 21, v29
	v_min3_u32 v80, v80, v81, v82
	v_or_b32_e32 v81, 22, v30
	v_or_b32_e32 v82, 23, v31
	v_min3_u32 v80, v80, v81, v82
	v_or_b32_e32 v81, 24, v32
	v_or_b32_e32 v82, 25, v33
	v_min3_u32 v80, v80, v81, v82
	v_or_b32_e32 v81, 26, v34
	v_or_b32_e32 v82, 27, v35
	v_min3_u32 v80, v80, v81, v82
	v_or_b32_e32 v81, 28, v36
	v_or_b32_e32 v82, 29, v37
	v_min3_u32 v80, v80, v81, v82
	v_or_b32_e32 v81, 30, v38
	v_or_b32_e32 v82, 31, v39
	v_min3_u32 v80, v80, v81, v82
	v_mul_f64 v[86:87], v[86:87], v[84:85]
	v_mul_f32_e32 v24, s14, v24
	v_mul_f32_e32 v25, s14, v25
	v_mul_f32_e32 v26, s14, v26
	v_mul_f32_e32 v27, s14, v27
	v_mul_f32_e32 v28, s14, v28
	v_mul_f32_e32 v29, s14, v29
	v_mul_f32_e32 v30, s14, v30
	v_mul_f32_e32 v31, s14, v31
	v_mul_f32_e32 v32, s14, v32
	v_mul_f32_e32 v33, s14, v33
	v_mul_f32_e32 v34, s14, v34
	v_mul_f32_e32 v35, s14, v35
	v_mul_f32_e32 v36, s14, v36
	v_mul_f32_e32 v37, s14, v37
	v_mul_f32_e32 v38, s14, v38
	v_mul_f32_e32 v39, s14, v39
	v_exp_f32_e32 v24, v24
	v_exp_f32_e32 v25, v25
	v_exp_f32_e32 v26, v26
	v_exp_f32_e32 v27, v27
	v_exp_f32_e32 v28, v28
	v_exp_f32_e32 v29, v29
	v_exp_f32_e32 v30, v30
	v_exp_f32_e32 v31, v31
	v_exp_f32_e32 v32, v32
	v_exp_f32_e32 v33, v33
	v_exp_f32_e32 v34, v34
	v_exp_f32_e32 v35, v35
	v_exp_f32_e32 v36, v36
	v_exp_f32_e32 v37, v37
	v_exp_f32_e32 v38, v38
	v_exp_f32_e32 v39, v39
	v_add_f32_e32 v78, v24, v26
	v_add_f32_e32 v79, v25, v27
	v_add_f32_e32 v78, v78, v28
	v_add_f32_e32 v79, v79, v29
	v_add_f32_e32 v78, v78, v30
	v_add_f32_e32 v79, v79, v31
	v_add_f32_e32 v78, v78, v32
	v_add_f32_e32 v79, v79, v33
	v_add_f32_e32 v78, v78, v34
	v_add_f32_e32 v79, v79, v35
	v_add_f32_e32 v78, v78, v36
	v_add_f32_e32 v79, v79, v37
	v_add_f32_e32 v78, v78, v38
	v_add_f32_e32 v79, v79, v39
	v_add_f32_e32 v78, v78, v79
	v_cvt_f64_f32_e32 v[84:85], v78
	v_cndmask_b32_e64 v75, v75, v80, s[20:21]
	v_mov_b32_e32 v73, v77
	v_add_f64 v[86:87], v[86:87], v[84:85]
	s_waitcnt vmcnt(17)
	v_max3_f32 v76, v40, v41, v42
	v_max3_f32 v76, v76, v43, v44
	v_max3_f32 v76, v76, v45, v46
	v_max3_f32 v76, v76, v47, v48
	v_max3_f32 v76, v76, v49, v50
	v_max3_f32 v76, v76, v51, v52
	v_max3_f32 v76, v76, v53, v54
	v_max_f32_e32 v76, v76, v55
	v_max_f32_e32 v77, v73, v76
	v_cmp_gt_f32_e64 s[20:21], v76, v73
	v_sub_f32_e32 v83, v73, v77
	v_mul_f32_e32 v83, s14, v83
	v_exp_f32_e32 v83, v83
	v_sub_f32_e32 v40, v40, v77
	v_sub_f32_e32 v41, v41, v77
	v_sub_f32_e32 v42, v42, v77
	v_sub_f32_e32 v43, v43, v77
	v_sub_f32_e32 v44, v44, v77
	v_sub_f32_e32 v45, v45, v77
	v_sub_f32_e32 v46, v46, v77
	v_sub_f32_e32 v47, v47, v77
	v_sub_f32_e32 v48, v48, v77
	v_sub_f32_e32 v49, v49, v77
	v_sub_f32_e32 v50, v50, v77
	v_sub_f32_e32 v51, v51, v77
	v_sub_f32_e32 v52, v52, v77
	v_sub_f32_e32 v53, v53, v77
	v_sub_f32_e32 v54, v54, v77
	v_sub_f32_e32 v55, v55, v77
	v_cvt_f64_f32_e32 v[84:85], v83
	v_or_b32_e32 v81, 32, v40
	v_or_b32_e32 v82, 33, v41
	v_min_u32_e32 v80, v81, v82
	v_or_b32_e32 v81, 34, v42
	v_or_b32_e32 v82, 35, v43
	v_min3_u32 v80, v80, v81, v82
	v_or_b32_e32 v81, 36, v44
	v_or_b32_e32 v82, 37, v45
	v_min3_u32 v80, v80, v81, v82
	v_or_b32_e32 v81, 38, v46
	v_or_b32_e32 v82, 39, v47
	v_min3_u32 v80, v80, v81, v82
	v_or_b32_e32 v81, 40, v48
	v_or_b32_e32 v82, 41, v49
	v_min3_u32 v80, v80, v81, v82
	v_or_b32_e32 v81, 42, v50
	v_or_b32_e32 v82, 43, v51
	v_min3_u32 v80, v80, v81, v82
	v_or_b32_e32 v81, 44, v52
	v_or_b32_e32 v82, 45, v53
	v_min3_u32 v80, v80, v81, v82
	v_or_b32_e32 v81, 46, v54
	v_or_b32_e32 v82, 47, v55
	v_min3_u32 v80, v80, v81, v82
	v_mul_f64 v[86:87], v[86:87], v[84:85]
	v_mul_f32_e32 v40, s14, v40
	v_mul_f32_e32 v41, s14, v41
	v_mul_f32_e32 v42, s14, v42
	v_mul_f32_e32 v43, s14, v43
	v_mul_f32_e32 v44, s14, v44
	v_mul_f32_e32 v45, s14, v45
	v_mul_f32_e32 v46, s14, v46
	v_mul_f32_e32 v47, s14, v47
	v_mul_f32_e32 v48, s14, v48
	v_mul_f32_e32 v49, s14, v49
	v_mul_f32_e32 v50, s14, v50
	v_mul_f32_e32 v51, s14, v51
	v_mul_f32_e32 v52, s14, v52
	v_mul_f32_e32 v53, s14, v53
	v_mul_f32_e32 v54, s14, v54
	v_mul_f32_e32 v55, s14, v55
	v_exp_f32_e32 v40, v40
	v_exp_f32_e32 v41, v41
	v_exp_f32_e32 v42, v42
	v_exp_f32_e32 v43, v43
	v_exp_f32_e32 v44, v44
	v_exp_f32_e32 v45, v45
	v_exp_f32_e32 v46, v46
	v_exp_f32_e32 v47, v47
	v_exp_f32_e32 v48, v48
	v_exp_f32_e32 v49, v49
	v_exp_f32_e32 v50, v50
	v_exp_f32_e32 v51, v51
	v_exp_f32_e32 v52, v52
	v_exp_f32_e32 v53, v53
	v_exp_f32_e32 v54, v54
	v_exp_f32_e32 v55, v55
	v_add_f32_e32 v78, v40, v42
	v_add_f32_e32 v79, v41, v43
	v_add_f32_e32 v78, v78, v44
	v_add_f32_e32 v79, v79, v45
	v_add_f32_e32 v78, v78, v46
	v_add_f32_e32 v79, v79, v47
	v_add_f32_e32 v78, v78, v48
	v_add_f32_e32 v79, v79, v49
	v_add_f32_e32 v78, v78, v50
	v_add_f32_e32 v79, v79, v51
	v_add_f32_e32 v78, v78, v52
	v_add_f32_e32 v79, v79, v53
	v_add_f32_e32 v78, v78, v54
	v_add_f32_e32 v79, v79, v55
	v_add_f32_e32 v78, v78, v79
	v_cvt_f64_f32_e32 v[84:85], v78
	v_cndmask_b32_e64 v75, v75, v80, s[20:21]
	v_mov_b32_e32 v73, v77
	v_add_f64 v[86:87], v[86:87], v[84:85]
	s_waitcnt vmcnt(5)
	v_max3_f32 v76, v56, v57, v58
	v_max3_f32 v76, v76, v59, v60
	v_max3_f32 v76, v76, v61, v62
	v_max3_f32 v76, v76, v63, v64
	v_max3_f32 v76, v76, v65, v66
	v_max_f32_e32 v76, v76, v67
	v_max_f32_e32 v77, v73, v76
	v_cmp_gt_f32_e64 s[20:21], v76, v73
	v_sub_f32_e32 v83, v73, v77
	v_mul_f32_e32 v83, s14, v83
	v_exp_f32_e32 v83, v83
	v_sub_f32_e32 v56, v56, v77
	v_sub_f32_e32 v57, v57, v77
	v_sub_f32_e32 v58, v58, v77
	v_sub_f32_e32 v59, v59, v77
	v_sub_f32_e32 v60, v60, v77
	v_sub_f32_e32 v61, v61, v77
	v_sub_f32_e32 v62, v62, v77
	v_sub_f32_e32 v63, v63, v77
	v_sub_f32_e32 v64, v64, v77
	v_sub_f32_e32 v65, v65, v77
	v_sub_f32_e32 v66, v66, v77
	v_sub_f32_e32 v67, v67, v77
	v_cvt_f64_f32_e32 v[84:85], v83
	v_or_b32_e32 v81, 48, v56
	v_or_b32_e32 v82, 49, v57
	v_min_u32_e32 v80, v81, v82
	v_or_b32_e32 v81, 50, v58
	v_or_b32_e32 v82, 51, v59
	v_min3_u32 v80, v80, v81, v82
	v_or_b32_e32 v81, 52, v60
	v_or_b32_e32 v82, 53, v61
	v_min3_u32 v80, v80, v81, v82
	v_or_b32_e32 v81, 54, v62
	v_or_b32_e32 v82, 55, v63
	v_min3_u32 v80, v80, v81, v82
	v_or_b32_e32 v81, 56, v64
	v_or_b32_e32 v82, 57, v65
	v_min3_u32 v80, v80, v81, v82
	v_or_b32_e32 v81, 58, v66
	v_or_b32_e32 v82, 59, v67
	v_min3_u32 v80, v80, v81, v82
	v_mul_f64 v[86:87], v[86:87], v[84:85]
	v_mul_f32_e32 v56, s14, v56
	v_mul_f32_e32 v57, s14, v57
	v_mul_f32_e32 v58, s14, v58
	v_mul_f32_e32 v59, s14, v59
	v_mul_f32_e32 v60, s14, v60
	v_mul_f32_e32 v61, s14, v61
	v_mul_f32_e32 v62, s14, v62
	v_mul_f32_e32 v63, s14, v63
	v_mul_f32_e32 v64, s14, v64
	v_mul_f32_e32 v65, s14, v65
	v_mul_f32_e32 v66, s14, v66
	v_mul_f32_e32 v67, s14, v67
	v_exp_f32_e32 v56, v56
	v_exp_f32_e32 v57, v57
	v_exp_f32_e32 v58, v58
	v_exp_f32_e32 v59, v59
	v_exp_f32_e32 v60, v60
	v_exp_f32_e32 v61, v61
	v_exp_f32_e32 v62, v62
	v_exp_f32_e32 v63, v63
	v_exp_f32_e32 v64, v64
	v_exp_f32_e32 v65, v65
	v_exp_f32_e32 v66, v66
	v_exp_f32_e32 v67, v67
	v_add_f32_e32 v78, v56, v58
	v_add_f32_e32 v79, v57, v59
	v_add_f32_e32 v78, v78, v60
	v_add_f32_e32 v79, v79, v61
	v_add_f32_e32 v78, v78, v62
	v_add_f32_e32 v79, v79, v63
	v_add_f32_e32 v78, v78, v64
	v_add_f32_e32 v79, v79, v65
	v_add_f32_e32 v78, v78, v66
	v_add_f32_e32 v79, v79, v67
	v_add_f32_e32 v78, v78, v79
	v_cvt_f64_f32_e32 v[84:85], v78
	v_cndmask_b32_e64 v75, v75, v80, s[20:21]
	v_mov_b32_e32 v73, v77
	v_add_f64 v[86:87], v[86:87], v[84:85]
	s_waitcnt vmcnt(0)
	v_max3_f32 v76, v68, v69, v70
	v_max3_f32 v76, v76, v71, v72
	v_max_f32_e32 v77, v73, v76
	v_cmp_gt_f32_e64 s[20:21], v76, v73
	v_sub_f32_e32 v83, v73, v77
	v_mul_f32_e32 v83, s14, v83
	v_exp_f32_e32 v83, v83
	v_sub_f32_e32 v68, v68, v77
	v_sub_f32_e32 v69, v69, v77
	v_sub_f32_e32 v70, v70, v77
	v_sub_f32_e32 v71, v71, v77
	v_sub_f32_e32 v72, v72, v77
	v_cvt_f64_f32_e32 v[84:85], v83
	v_or_b32_e32 v81, 60, v68
	v_or_b32_e32 v82, 61, v69
	v_min_u32_e32 v80, v81, v82
	v_or_b32_e32 v81, 62, v70
	v_or_b32_e32 v82, 63, v71
	v_min3_u32 v80, v80, v81, v82
	v_or_b32_e32 v81, 64, v72
	v_min_u32_e32 v80, v80, v81
	v_mul_f64 v[86:87], v[86:87], v[84:85]
	v_mul_f32_e32 v68, s14, v68
	v_mul_f32_e32 v69, s14, v69
	v_mul_f32_e32 v70, s14, v70
	v_mul_f32_e32 v71, s14, v71
	v_mul_f32_e32 v72, s14, v72
	v_exp_f32_e32 v68, v68
	v_exp_f32_e32 v69, v69
	v_exp_f32_e32 v70, v70
	v_exp_f32_e32 v71, v71
	v_exp_f32_e32 v72, v72
	v_add_f32_e32 v78, v68, v70
	v_add_f32_e32 v79, v69, v71
	v_add_f32_e32 v78, v78, v72
	v_add_f32_e32 v78, v78, v79
	v_cvt_f64_f32_e32 v[84:85], v78
	v_cndmask_b32_e64 v75, v75, v80, s[20:21]
	v_mov_b32_e32 v73, v77
	v_add_f64 v[86:87], v[86:87], v[84:85]
	v_rcp_f64_e32 v[88:89], v[86:87]
	v_cmp_gt_u32_e32 vcc, 64, v75
	s_and_b64 vcc, vcc, s[36:37]
	v_fma_f64 v[90:91], -v[86:87], v[88:89], 1.0
	v_fma_f64 v[88:89], v[90:91], v[88:89], v[88:89]
	v_cvt_f32_f64_e32 v3, v[88:89]
	v_cndmask_b32_e32 v74, 0, v3, vcc
	global_store_dwordx2 v98, v[74:75], s[6:7]

	.amdhsa_kernel _Z12score_kernelPKfP15HIP_vector_typeIjLj2EES0_S0_
		.amdhsa_group_segment_fixed_size 0
		.amdhsa_private_segment_fixed_size 0
		.amdhsa_kernarg_size 32
		.amdhsa_user_sgpr_count 2
		.amdhsa_user_sgpr_dispatch_ptr 0
		.amdhsa_user_sgpr_queue_ptr 0
		.amdhsa_user_sgpr_kernarg_segment_ptr 1
		.amdhsa_user_sgpr_dispatch_id 0
		.amdhsa_user_sgpr_kernarg_preload_length 0
		.amdhsa_user_sgpr_kernarg_preload_offset 0
		.amdhsa_user_sgpr_private_segment_size 0
		.amdhsa_uses_dynamic_stack 0
		.amdhsa_enable_private_segment 0
		.amdhsa_system_sgpr_workgroup_id_x 1
		.amdhsa_system_sgpr_workgroup_id_y 0
		.amdhsa_system_sgpr_workgroup_id_z 0
		.amdhsa_system_sgpr_workgroup_info 0
		.amdhsa_system_vgpr_workitem_id 0
		.amdhsa_next_free_vgpr 100
		.amdhsa_next_free_sgpr 56
		.amdhsa_accum_offset 100
		.amdhsa_reserve_vcc 1
		.amdhsa_float_round_mode_32 0
		.amdhsa_float_round_mode_16_64 0
		.amdhsa_float_denorm_mode_32 3
		.amdhsa_float_denorm_mode_16_64 3
		.amdhsa_dx10_clamp 1
		.amdhsa_ieee_mode 1
		.amdhsa_fp16_overflow 0
		.amdhsa_tg_split 0
		.amdhsa_exception_fp_ieee_invalid_op 0
		.amdhsa_exception_fp_denorm_src 0
		.amdhsa_exception_fp_ieee_div_zero 0
		.amdhsa_exception_fp_ieee_overflow 0
		.amdhsa_exception_fp_ieee_underflow 0
		.amdhsa_exception_fp_ieee_inexact 0
		.amdhsa_exception_int_div_zero 0
	.end_amdhsa_kernel

amdhsa.kernels:
  - .agpr_count:     0
    .args:
      - .actual_access:  read_only
        .address_space:  global
        .offset:         0
        .size:           8
        .value_kind:     global_buffer
      - .actual_access:  write_only
        .address_space:  global
        .offset:         8
        .size:           8
        .value_kind:     global_buffer
      - .actual_access:  read_only
        .address_space:  global
        .offset:         16
        .size:           8
        .value_kind:     global_buffer
      - .actual_access:  read_only
        .address_space:  global
        .offset:         24
        .size:           8
        .value_kind:     global_buffer
    .group_segment_fixed_size: 0
    .kernarg_segment_align: 8
    .kernarg_segment_size: 32
    .language:       OpenCL C
    .language_version:
      - 2
      - 0
    .max_flat_workgroup_size: 640
    .name:           _Z12score_kernelPKfP15HIP_vector_typeIjLj2EES0_S0_
    .private_segment_fixed_size: 0
    .sgpr_count:     62
    .sgpr_spill_count: 0
    .symbol:         _Z12score_kernelPKfP15HIP_vector_typeIjLj2EES0_S0_.kd
    .uniform_work_group_size: 1
    .uses_dynamic_stack: false
    .vgpr_count:     100
    .vgpr_spill_count: 0
    .wavefront_size: 64
  - .agpr_count:     0
    .args:
      - .actual_access:  read_only
        .address_space:  global
        .offset:         0
        .size:           8
        .value_kind:     global_buffer
      - .actual_access:  read_only
        .address_space:  global
        .offset:         8
        .size:           8
        .value_kind:     global_buffer
      - .actual_access:  write_only
        .address_space:  global
        .offset:         16
        .size:           8
        .value_kind:     global_buffer
    .group_segment_fixed_size: 49664
    .kernarg_segment_align: 8
    .kernarg_segment_size: 24
    .language:       OpenCL C
    .language_version:
      - 2
      - 0
    .max_flat_workgroup_size: 1024
    .name:           _Z13select_kernelPK15HIP_vector_typeIjLj2EEPKfPf
    .private_segment_fixed_size: 0
    .sgpr_count:     58
    .sgpr_spill_count: 0
    .symbol:         _Z13select_kernelPK15HIP_vector_typeIjLj2EEPKfPf.kd
    .uniform_work_group_size: 1
    .uses_dynamic_stack: false
    .vgpr_count:     57
    .vgpr_spill_count: 0
    .wavefront_size: 64
